# baseline (speedup 1.0000x reference)
.LBB2_30:
	s_or_b64 exec, exec, s[4:5]
	v_readfirstlane_b32 s6, v17
	s_cmp_lg_u32 s6, 4
	s_cbranch_scc1 .Lsp_skip
	s_waitcnt vmcnt(0)
	v_add_f32_dpp v54, v9, v9 quad_perm:[1,0,3,2] row_mask:0xf bank_mask:0xf bound_ctrl:1
	v_add_f32_dpp v55, v8, v8 quad_perm:[1,0,3,2] row_mask:0xf bank_mask:0xf bound_ctrl:1
	s_nop 0
	v_add_f32_dpp v54, v54, v54 quad_perm:[2,3,0,1] row_mask:0xf bank_mask:0xf bound_ctrl:1
	v_add_f32_dpp v55, v55, v55 quad_perm:[2,3,0,1] row_mask:0xf bank_mask:0xf bound_ctrl:1
	s_nop 0
	v_add_f32_dpp v54, v54, v54 row_half_mirror row_mask:0xf bank_mask:0xf bound_ctrl:1
	v_add_f32_dpp v55, v55, v55 row_half_mirror row_mask:0xf bank_mask:0xf bound_ctrl:1
	s_nop 0
	v_add_f32_dpp v54, v54, v54 row_mirror row_mask:0xf bank_mask:0xf bound_ctrl:1
	v_add_f32_dpp v55, v55, v55 row_mirror row_mask:0xf bank_mask:0xf bound_ctrl:1
	s_nop 0
	v_readlane_b32 s6, v54, 0
	v_readlane_b32 s8, v54, 16
	v_readlane_b32 s7, v54, 32
	v_readlane_b32 s9, v54, 48
	v_readlane_b32 s10, v55, 0
	v_readlane_b32 s12, v55, 16
	v_readlane_b32 s11, v55, 32
	v_readlane_b32 s13, v55, 48
	v_mov_b32_e32 v56, s8
	v_mov_b32_e32 v57, s9
	v_pk_add_f32 v[56:57], s[6:7], v[56:57]
	v_mov_b32_e32 v58, s12
	v_mov_b32_e32 v59, s13
	v_pk_add_f32 v[58:59], s[10:11], v[58:59]
	v_add_f32_e32 v56, v56, v57
	v_add_f32_e32 v57, v58, v59
	s_mov_b32 s3, 0x41200000
	v_div_scale_f32 v58, s[12:13], s3, s3, v57
	v_rcp_f32_e32 v59, v58
	s_nop 0
	v_fma_f32 v60, -v58, v59, 1.0
	v_fmac_f32_e32 v59, v60, v59
	v_div_scale_f32 v60, vcc, v57, s3, v57
	v_mul_f32_e32 v61, v60, v59
	v_fma_f32 v62, -v58, v61, v60
	v_fmac_f32_e32 v61, v62, v59
	v_fma_f32 v58, -v58, v61, v60
	v_div_scale_f32 v60, s[12:13], s3, s3, v56
	v_rcp_f32_e32 v62, v60
	v_div_fmas_f32 v58, v58, v59, v61
	v_div_fixup_f32 v57, v58, s3, v57
	s_mov_b32 s14, 0x322bcc77
	v_fma_f32 v58, -v60, v62, 1.0
	v_fmac_f32_e32 v62, v58, v62
	v_div_scale_f32 v58, vcc, v56, s3, v56
	v_mul_f32_e32 v59, v58, v62
	v_fma_f32 v61, -v60, v59, v58
	v_fmac_f32_e32 v59, v61, v62
	v_fma_f32 v58, -v60, v59, v58
	v_div_fmas_f32 v58, v58, v62, v59
	v_div_fixup_f32 v56, v58, s3, v56
	v_pk_add_f32 v[56:57], v[56:57], s[14:15] op_sel_hi:[1,0]
	s_nop 0
	v_div_scale_f32 v58, s[12:13], v57, v57, v8
	v_rcp_f32_e32 v59, v58
	s_nop 0
	v_fma_f32 v60, -v58, v59, 1.0
	v_fmac_f32_e32 v59, v60, v59
	v_div_scale_f32 v60, vcc, v8, v57, v8
	v_mul_f32_e32 v61, v60, v59
	v_fma_f32 v62, -v58, v61, v60
	v_fmac_f32_e32 v61, v62, v59
	v_fma_f32 v58, -v58, v61, v60
	v_div_scale_f32 v60, s[12:13], v56, v56, v9
	v_rcp_f32_e32 v62, v60
	v_div_fmas_f32 v58, v58, v59, v61
	v_div_fixup_f32 v57, v58, v57, v8
	v_fma_f32 v58, -v60, v62, 1.0
	v_fmac_f32_e32 v62, v58, v62
	v_div_scale_f32 v58, vcc, v9, v56, v9
	v_mul_f32_e32 v59, v58, v62
	v_fma_f32 v61, -v60, v59, v58
	v_fmac_f32_e32 v59, v61, v62
	v_fma_f32 v58, -v60, v59, v58
	v_div_fmas_f32 v58, v58, v62, v59
	v_div_fixup_f32 v56, v58, v56, v9
	v_sub_f32_e32 v56, v56, v57
	v_mul_f32_e32 v57, 0.5, v56
	v_mul_f32_e32 v56, v56, v57
	v_div_scale_f32 v57, s[12:13], s3, s3, v56
	v_rcp_f32_e32 v58, v57
	s_nop 0
	v_fma_f32 v59, -v57, v58, 1.0
	v_fmac_f32_e32 v58, v59, v58
	v_div_scale_f32 v59, vcc, v56, s3, v56
	v_mul_f32_e32 v60, v59, v58
	v_fma_f32 v61, -v57, v60, v59
	v_fmac_f32_e32 v60, v61, v58
	v_fma_f32 v57, -v57, v60, v59
	v_div_fmas_f32 v57, v57, v58, v60
	v_div_fixup_f32 v56, v57, s3, v56
	s_nop 1
	v_add_f32_dpp v56, v56, v56 quad_perm:[1,0,3,2] row_mask:0xf bank_mask:0xf bound_ctrl:1
	s_nop 1
	v_add_f32_dpp v56, v56, v56 quad_perm:[2,3,0,1] row_mask:0xf bank_mask:0xf bound_ctrl:1
	s_nop 1
	v_add_f32_dpp v56, v56, v56 row_half_mirror row_mask:0xf bank_mask:0xf bound_ctrl:1
	s_nop 1
	v_add_f32_dpp v56, v56, v56 row_mirror row_mask:0xf bank_mask:0xf bound_ctrl:1
	s_nop 0
	v_readlane_b32 s6, v56, 0
	v_readlane_b32 s8, v56, 16
	v_readlane_b32 s7, v56, 32
	v_readlane_b32 s9, v56, 48
	v_cmp_eq_u32_e32 vcc, 0, v1
	s_nop 1
	v_mov_b32_e32 v56, s8
	v_mov_b32_e32 v57, s9
	v_pk_add_f32 v[56:57], s[6:7], v[56:57]
	s_nop 0
	v_add_f32_e32 v56, v56, v57
	s_and_saveexec_b64 s[6:7], vcc
	v_mov_b32_e32 v57, 0
	global_atomic_add_f32 v57, v56, s[28:29]
	s_mov_b64 exec, s[6:7]
.Lsp_skip:
	s_movk_i32 s3, 0x64
	v_cmp_gt_u32_e64 s[4:5], s3, v0
	s_movk_i32 s6, 0x100
	v_cmp_gt_u32_e32 vcc, s6, v0
	v_cndmask_b32_e64 v4, 0, v0, s[4:5]
	v_lshlrev_b32_e32 v2, 2, v4
	s_waitcnt vmcnt(0) lgkmcnt(0)
	v_mov_b32_e32 v6, v66
	v_mov_b32_e32 v7, v67
	s_and_saveexec_b64 s[34:35], vcc
	s_cbranch_execz .LBB2_32
	v_lshlrev_b32_e32 v2, 2, v0
	s_mov_b64 s[20:21], s[40:41]
	s_mov_b64 s[22:23], s[42:43]
	s_mov_b64 s[24:25], s[44:45]
	s_mov_b64 s[26:27], s[46:47]
	s_mov_b64 s[36:37], s[48:49]
	v_mov_b32_e32 v5, v56
	v_mov_b32_e32 v14, v57
	v_mov_b32_e32 v15, v58
	v_mov_b32_e32 v16, v59
	v_mov_b32_e32 v3, v60
	v_mov_b32_e32 v18, v61
	v_mov_b32_e32 v19, v62
	v_mov_b32_e32 v20, v63
	v_mov_b32_e32 v21, v64
	v_mov_b32_e32 v22, v65
	v_cvt_f32_i32_e32 v10, s20
	v_cvt_f32_i32_e32 v11, s21
	v_cvt_f32_i32_e32 v12, s22
	v_cvt_f32_i32_e32 v13, s23
	v_cvt_f32_i32_e32 v23, s24
	s_waitcnt vmcnt(9)
	v_div_scale_f32 v24, s[6:7], v10, v10, v5
	s_waitcnt vmcnt(8)
	v_div_scale_f32 v26, s[6:7], v11, v11, v14
	v_rcp_f32_e32 v32, v24
	s_waitcnt vmcnt(7)
	v_div_scale_f32 v28, s[8:9], v12, v12, v15
	v_rcp_f32_e32 v33, v26
	v_rcp_f32_e32 v34, v28
	v_fma_f32 v39, -v24, v32, 1.0
	v_div_scale_f32 v25, vcc, v5, v10, v5
	s_waitcnt vmcnt(6)
	v_div_scale_f32 v30, s[10:11], v13, v13, v16
	v_fma_f32 v40, -v26, v33, 1.0
	v_fmac_f32_e32 v32, v39, v32
	v_div_scale_f32 v27, s[6:7], v14, v11, v14
	v_rcp_f32_e32 v35, v30
	v_fma_f32 v41, -v28, v34, 1.0
	v_fmac_f32_e32 v33, v40, v33
	v_mul_f32_e32 v39, v25, v32
	v_div_scale_f32 v29, s[8:9], v15, v12, v15
	v_fmac_f32_e32 v34, v41, v34
	v_mul_f32_e32 v40, v27, v33
	v_fma_f32 v43, -v24, v39, v25
	v_mul_f32_e32 v41, v29, v34
	v_fma_f32 v44, -v26, v40, v27
	v_fmac_f32_e32 v39, v43, v32
	v_fma_f32 v45, -v28, v41, v29
	v_fmac_f32_e32 v40, v44, v33
	v_fma_f32 v24, -v24, v39, v25
	s_waitcnt vmcnt(5)
	v_div_scale_f32 v36, s[12:13], v23, v23, v3
	v_fma_f32 v42, -v30, v35, 1.0
	v_fmac_f32_e32 v41, v45, v34
	v_fma_f32 v25, -v26, v40, v27
	v_div_fmas_f32 v24, v24, v32, v39
	s_mov_b64 vcc, s[6:7]
	v_div_scale_f32 v31, s[10:11], v16, v13, v16
	v_rcp_f32_e32 v38, v36
	v_fmac_f32_e32 v35, v42, v35
	v_fma_f32 v26, -v28, v41, v29
	v_div_fixup_f32 v5, v24, v10, v5
	v_div_fmas_f32 v10, v25, v33, v40
	s_mov_b64 vcc, s[8:9]
	v_mul_f32_e32 v42, v31, v35
	v_div_fixup_f32 v10, v10, v11, v14
	v_div_fmas_f32 v11, v26, v34, v41
	v_fma_f32 v46, -v30, v42, v31
	v_div_fixup_f32 v11, v11, v12, v15
	v_cvt_f32_i32_e32 v15, s25
	v_fmac_f32_e32 v42, v46, v35
	v_fma_f32 v47, -v36, v38, 1.0
	v_fma_f32 v27, -v30, v42, v31
	v_add_f32_e32 v24, 0, v5
	s_mov_b64 vcc, s[10:11]
	v_div_scale_f32 v37, s[12:13], v3, v23, v3
	v_fmac_f32_e32 v38, v47, v38
	v_add_f32_e32 v14, v24, v10
	v_div_fmas_f32 v12, v27, v35, v42
	v_mul_f32_e32 v28, v37, v38
	v_add_f32_e32 v14, v14, v11
	v_div_fixup_f32 v12, v12, v13, v16
	s_waitcnt vmcnt(4)
	v_div_scale_f32 v16, s[6:7], v15, v15, v18
	v_add_f32_e32 v13, v14, v12
	v_fma_f32 v14, -v36, v28, v37
	v_rcp_f32_e32 v24, v16
	v_fmac_f32_e32 v28, v14, v38
	v_fma_f32 v14, -v36, v28, v37
	s_mov_b64 vcc, s[12:13]
	v_div_fmas_f32 v14, v14, v38, v28
	v_div_fixup_f32 v3, v14, v23, v3
	v_fma_f32 v14, -v16, v24, 1.0
	v_fmac_f32_e32 v24, v14, v24
	v_div_scale_f32 v14, vcc, v18, v15, v18
	v_cvt_f32_i32_e32 v26, s26
	v_mul_f32_e32 v23, v14, v24
	v_fma_f32 v25, -v16, v23, v14
	v_fmac_f32_e32 v23, v25, v24
	v_fma_f32 v14, -v16, v23, v14
	s_waitcnt vmcnt(3)
	v_div_scale_f32 v16, s[6:7], v26, v26, v19
	v_rcp_f32_e32 v25, v16
	v_div_fmas_f32 v14, v14, v24, v23
	v_div_fixup_f32 v14, v14, v15, v18
	v_cvt_f32_i32_e32 v24, s27
	v_fma_f32 v15, -v16, v25, 1.0
	v_fmac_f32_e32 v25, v15, v25
	v_div_scale_f32 v15, vcc, v19, v26, v19
	v_mul_f32_e32 v18, v15, v25
	v_fma_f32 v23, -v16, v18, v15
	v_fmac_f32_e32 v18, v23, v25
	v_fma_f32 v15, -v16, v18, v15
	s_waitcnt vmcnt(2)
	v_div_scale_f32 v16, s[6:7], v24, v24, v20
	v_rcp_f32_e32 v23, v16
	v_div_fmas_f32 v15, v15, v25, v18
	v_div_fixup_f32 v15, v15, v26, v19
	v_cvt_f32_i32_e32 v26, s36
	v_fma_f32 v18, -v16, v23, 1.0
	v_fmac_f32_e32 v23, v18, v23
	v_div_scale_f32 v18, vcc, v20, v24, v20
	v_mul_f32_e32 v19, v18, v23
	v_fma_f32 v25, -v16, v19, v18
	v_fmac_f32_e32 v19, v25, v23
	v_fma_f32 v16, -v16, v19, v18
	s_waitcnt vmcnt(1)
	v_div_scale_f32 v18, s[6:7], v26, v26, v21
	v_rcp_f32_e32 v25, v18
	v_div_fmas_f32 v16, v16, v23, v19
	v_div_fixup_f32 v16, v16, v24, v20
	v_cvt_f32_i32_e32 v24, s37
	v_fma_f32 v19, -v18, v25, 1.0
	v_fmac_f32_e32 v25, v19, v25
	v_div_scale_f32 v19, vcc, v21, v26, v21
	v_mul_f32_e32 v20, v19, v25
	v_fma_f32 v23, -v18, v20, v19
	v_fmac_f32_e32 v20, v23, v25
	v_fma_f32 v18, -v18, v20, v19
	s_waitcnt vmcnt(0)
	v_div_scale_f32 v19, s[6:7], v24, v24, v22
	v_rcp_f32_e32 v23, v19
	v_div_fmas_f32 v18, v18, v25, v20
	v_div_fixup_f32 v18, v18, v26, v21
	v_add_f32_e32 v13, v13, v3
	v_fma_f32 v20, -v19, v23, 1.0
	v_fmac_f32_e32 v23, v20, v23
	v_div_scale_f32 v20, vcc, v22, v24, v22
	v_mul_f32_e32 v21, v20, v23
	v_fma_f32 v25, -v19, v21, v20
	v_add_f32_e32 v13, v13, v14
	v_fmac_f32_e32 v21, v25, v23
	v_add_f32_e32 v13, v13, v15
	v_fma_f32 v19, -v19, v21, v20
	v_add_f32_e32 v13, v13, v16
	v_div_fmas_f32 v19, v19, v23, v21
	v_add_f32_e32 v13, v13, v18
	v_div_fixup_f32 v19, v19, v24, v22
	v_add_f32_e32 v13, v13, v19
	s_mov_b32 s8, 0x41200000
	v_div_scale_f32 v20, s[6:7], s8, s8, v13
	v_rcp_f32_e32 v21, v20
	ds_write_b32 v2, v5
	v_fma_f32 v22, -v20, v21, 1.0
	v_fmac_f32_e32 v21, v22, v21
	v_div_scale_f32 v22, vcc, v13, s8, v13
	v_mul_f32_e32 v23, v22, v21
	v_fma_f32 v24, -v20, v23, v22
	v_fmac_f32_e32 v23, v24, v21
	v_fma_f32 v20, -v20, v23, v22
	v_div_fmas_f32 v20, v20, v21, v23
	v_div_fixup_f32 v13, v20, s8, v13
	v_sub_f32_e32 v5, v5, v13
	ds_write_b32 v2, v5 offset:10400
	ds_write_b32 v2, v10 offset:1040
	v_sub_f32_e32 v5, v10, v13
	ds_write_b32 v2, v5 offset:11440
	ds_write_b32 v2, v11 offset:2080
	v_sub_f32_e32 v5, v11, v13
	ds_write_b32 v2, v5 offset:12480
	ds_write_b32 v2, v12 offset:3120
	v_sub_f32_e32 v5, v12, v13
	ds_write_b32 v2, v5 offset:13520
	ds_write_b32 v2, v3 offset:4160
	v_sub_f32_e32 v3, v3, v13
	ds_write_b32 v2, v3 offset:14560
	ds_write_b32 v2, v14 offset:5200
	v_sub_f32_e32 v3, v14, v13
	ds_write_b32 v2, v3 offset:15600
	ds_write_b32 v2, v15 offset:6240
	v_sub_f32_e32 v3, v15, v13
	ds_write_b32 v2, v3 offset:16640
	ds_write_b32 v2, v16 offset:7280
	v_sub_f32_e32 v3, v16, v13
	ds_write_b32 v2, v3 offset:17680
	ds_write_b32 v2, v18 offset:8320
	v_sub_f32_e32 v3, v18, v13
	ds_write_b32 v2, v3 offset:18720
	ds_write_b32 v2, v19 offset:9360
	v_sub_f32_e32 v3, v19, v13
	ds_write_b32 v2, v3 offset:19760
.LBB2_32:
	s_or_b64 exec, exec, s[34:35]
	s_waitcnt lgkmcnt(0)
	s_barrier
	v_lshlrev_b32_e32 v10, 2, v0
	s_mov_b64 s[0:1], 0
	v_readfirstlane_b32 s3, v17
	s_cmp_gt_u32 s3, 7
	s_cbranch_scc1 .Lmf_skip
	v_and_b32_e32 v2, 15, v1
	v_lshrrev_b32_e32 v3, 4, v1
	v_mul_u32_u24_e32 v5, 0x410, v2
	v_lshl_add_u32 v5, v3, 5, v5
	s_lshl_b32 s8, s3, 7
	s_lshl_b32 s9, s3, 9
	s_add_u32 s9, s9, 0x5140
	v_add_u32_e32 v5, s8, v5
	ds_read_b128 v[18:21], v5
	ds_read_b128 v[26:29], v5 offset:10400
	ds_read_b128 v[22:25], v5 offset:16
	ds_read_b128 v[30:33], v5 offset:10416
	v_mul_u32_u24_e32 v11, 0xa0, v3
	v_lshl_add_u32 v11, v2, 2, v11
	v_add_u32_e32 v11, s9, v11
	v_cmp_gt_u32_e64 s[10:11], 10, v2
	v_cmp_gt_u32_e64 s[12:13], 3, v3
	v_cmp_gt_u32_e64 s[14:15], 2, v3
	s_and_b64 s[12:13], s[10:11], s[12:13]
	s_and_b64 s[14:15], s[10:11], s[14:15]
	s_waitcnt lgkmcnt(3)
	v_mfma_f32_16x16x4_f32 v[34:37], v18, v18, 0
	s_waitcnt lgkmcnt(2)
	v_mfma_f32_16x16x4_f32 v[38:41], v26, v26, 0
	v_mfma_f32_16x16x4_f32 v[34:37], v19, v19, v[34:37]
	v_mfma_f32_16x16x4_f32 v[38:41], v27, v27, v[38:41]
	v_mfma_f32_16x16x4_f32 v[34:37], v20, v20, v[34:37]
	v_mfma_f32_16x16x4_f32 v[38:41], v28, v28, v[38:41]
	v_mfma_f32_16x16x4_f32 v[34:37], v21, v21, v[34:37]
	v_mfma_f32_16x16x4_f32 v[38:41], v29, v29, v[38:41]
	s_waitcnt lgkmcnt(0)
	v_mfma_f32_16x16x4_f32 v[34:37], v22, v22, v[34:37]
	v_mfma_f32_16x16x4_f32 v[38:41], v30, v30, v[38:41]
	v_mfma_f32_16x16x4_f32 v[34:37], v23, v23, v[34:37]
	v_mfma_f32_16x16x4_f32 v[38:41], v31, v31, v[38:41]
	v_mfma_f32_16x16x4_f32 v[34:37], v24, v24, v[34:37]
	v_mfma_f32_16x16x4_f32 v[38:41], v32, v32, v[38:41]
	v_mfma_f32_16x16x4_f32 v[34:37], v25, v25, v[34:37]
	v_mfma_f32_16x16x4_f32 v[38:41], v33, v33, v[38:41]
	s_nop 11
	s_mov_b64 s[6:7], exec
	s_mov_b64 exec, s[12:13]
	ds_write_b32 v11, v34
	ds_write_b32 v11, v35 offset:40
	ds_write_b32 v11, v38 offset:4096
	ds_write_b32 v11, v39 offset:4136
	s_mov_b64 exec, s[14:15]
	ds_write_b32 v11, v36 offset:80
	ds_write_b32 v11, v37 offset:120
	ds_write_b32 v11, v40 offset:4176
	ds_write_b32 v11, v41 offset:4216
	s_mov_b64 exec, s[6:7]
